# rwkv token shift: waves with all previous and next tokens present run a copy without the missing-row selects
# speedup vs baseline: 1.0108x; 1.0034x over previous
.LBB0_391:
	s_ashr_i32 s0, s18, 5
	s_lshl_b32 s1, s0, 6
	s_add_i32 s8, s1, 0x7fffe000
	s_and_b32 s8, s8, 0x7fffff00
	s_addk_i32 s8, 0x2000
	s_and_b32 s9, s1, 0xfffff000
	s_cmpk_lt_i32 s0, 0x80
	v_mov_b32_e32 v103, v92
	s_cselect_b32 s0, s75, 0xc0
	s_movk_i32 s41, 0x1000
	s_cselect_b32 s8, s9, s8
	s_cselect_b32 s10, s41, 0x100
	s_and_b32 s0, s0, s1
	v_ashrrev_i32_e32 v142, 3, v103
	v_add_u32_e32 v2, s0, v142
	v_readlane_b32 s0, v255, 4
	v_readlane_b32 s1, v255, 5
	v_add_u32_e32 v96, s8, v2
	v_lshlrev_b32_e32 v3, 4, v103
	v_mov_b64_e32 v[0:1], s[0:1]
	s_movk_i32 s0, 0x2c00
	v_mad_i64_i32 v[0:1], s[0:1], v96, s0, v[0:1]
	v_and_b32_e32 v104, 0x70, v3
	v_lshl_add_u64 v[0:1], v[0:1], 0, v[104:105]
	s_mov_b64 s[0:1], 0x21301000
	v_lshl_add_u64 v[12:13], v[0:1], 0, s[0:1]
	s_lshl_b32 s28, s40, 7
	v_lshl_add_u64 v[14:15], v[12:13], 0, s[28:29]
	v_add_co_u32_e32 v0, vcc, s41, v14
	global_load_dwordx4 v[44:47], v[14:15], off offset:2048
	s_nop 0
	v_addc_co_u32_e32 v1, vcc, 0, v15, vcc
	global_load_dwordx4 v[28:31], v[0:1], off
	v_add_u32_e32 v0, 1, v2
	v_cmp_lt_i32_e64 s[8:9], 0, v2
	v_cmp_gt_i32_e64 s[10:11], s10, v0
	v_and_b32_e32 v137, 7, v103
	v_cndmask_b32_e64 v49, 0, -1, s[8:9]
	v_cndmask_b32_e64 v48, 0, v185, s[8:9]
	v_cndmask_b32_e64 v104, 0, v186, s[10:11]
	v_lshlrev_b32_e32 v56, 5, v137
	s_lshl_b32 s28, s26, 7
	v_lshl_add_u64 v[16:17], v[14:15], 0, v[48:49]
	v_lshl_add_u64 v[36:37], v[14:15], 0, v[104:105]
	v_add_u32_e32 v4, v112, v56
	v_add_u32_e32 v8, v115, v56
	s_mov_b64 s[12:13], 0x1000
	v_lshl_add_u64 v[40:41], v[12:13], 0, s[28:29]
	global_load_dwordx4 v[148:151], v[16:17], off offset:2048
	global_load_dwordx4 v[152:155], v[36:37], off offset:2048
	v_add_u32_e32 v57, v116, v56
	ds_read_b128 v[20:23], v4
	ds_read_b128 v[0:3], v4 offset:16
	ds_read_b128 v[24:27], v4 offset:256
	ds_read_b128 v[4:7], v4 offset:272
	ds_read_b128 v[80:83], v8
	ds_read_b128 v[72:75], v8 offset:16
	ds_read_b128 v[84:87], v8 offset:256
	ds_read_b128 v[76:79], v8 offset:272
	ds_read_b128 v[60:63], v57
	ds_read_b128 v[32:35], v57 offset:16
	s_lshl_b32 s0, s40, 8
	global_load_dwordx4 v[8:11], v[14:15], off
	v_lshl_add_u64 v[38:39], v[14:15], 0, s[12:13]
	global_load_dwordx4 v[16:19], v[16:17], off
	s_nop 0
	global_load_dwordx4 v[12:15], v[36:37], off
	s_mov_b64 s[12:13], 0x1800
	v_add_co_u32_e32 v36, vcc, s41, v40
	s_add_u32 s0, s7, s0
	v_lshl_add_u64 v[50:51], v[40:41], 0, s[12:13]
	v_addc_co_u32_e32 v37, vcc, 0, v41, vcc
	s_mov_b64 s[12:13], 0x1900
	v_lshl_add_u64 v[168:169], v[40:41], 0, s[12:13]
	s_addc_u32 s1, s4, 0
	v_lshl_add_u64 v[52:53], v[38:39], 0, v[48:49]
	v_lshl_add_u64 v[54:55], v[38:39], 0, v[104:105]
	global_load_dwordx4 v[40:43], v[36:37], off offset:2048
	global_load_dwordx4 v[64:67], v[52:53], off
	s_nop 0
	global_load_dwordx4 v[36:39], v[36:37], off offset:2304
	s_nop 0
	global_load_dwordx4 v[68:71], v[54:55], off
	global_load_dwordx4 v[156:159], v56, s[0:1] offset:16
	global_load_dwordx4 v[160:163], v56, s[0:1]
	ds_read_b128 v[164:167], v57 offset:256
	ds_read_b128 v[88:91], v57 offset:272
	s_cmp_eq_u32 s26, 0
	s_cselect_b64 s[12:13], -1, 0
	s_mov_b64 s[0:1], -1
	s_and_b64 vcc, exec, s[12:13]
	s_waitcnt vmcnt(12)
	v_lshlrev_b32_e32 v146, 16, v44
	v_and_b32_e32 v145, 0xffff0000, v44
	v_lshlrev_b32_e32 v144, 16, v45
	s_waitcnt vmcnt(11)
	v_lshlrev_b32_e32 v98, 16, v28
	v_and_b32_e32 v95, 0xffff0000, v28
	v_lshlrev_b32_e32 v100, 16, v29
	v_and_b32_e32 v99, 0xffff0000, v29
	v_lshl_add_u64 v[28:29], v[50:51], 0, v[48:49]
	v_and_b32_e32 v143, 0xffff0000, v45
	v_lshl_add_u64 v[44:45], v[50:51], 0, v[104:105]
	global_load_dwordx4 v[52:55], v[28:29], off
	global_load_dwordx4 v[56:59], v[44:45], off
	v_lshl_add_u64 v[28:29], v[168:169], 0, v[48:49]
	v_lshl_add_u64 v[48:49], v[168:169], 0, v[104:105]
	v_lshlrev_b32_e32 v141, 16, v46
	v_and_b32_e32 v140, 0xffff0000, v46
	v_lshlrev_b32_e32 v139, 16, v47
	v_and_b32_e32 v138, 0xffff0000, v47
	global_load_dwordx4 v[44:47], v[28:29], off
	s_nop 0
	global_load_dwordx4 v[48:51], v[48:49], off
	v_lshlrev_b32_e32 v102, 16, v30
	v_and_b32_e32 v101, 0xffff0000, v30
	s_waitcnt vmcnt(14)
	v_and_b32_e32 v30, 0xffff0000, v148
	v_lshlrev_b32_e32 v28, 16, v148
	s_and_b64 s[100:101], s[8:9], s[10:11]
	s_cmp_eq_u64 s[100:101], exec
	s_cbranch_scc1 .Lfp1
	v_cndmask_b32_e64 v30, 0, v30, s[8:9]
	s_waitcnt vmcnt(13)
	v_and_b32_e32 v97, 0xffff0000, v152
	v_cndmask_b32_e64 v28, 0, v28, s[8:9]
	v_lshlrev_b32_e32 v29, 16, v152
	v_cndmask_b32_e64 v97, 0, v97, s[10:11]
	v_sub_f32_e32 v30, v30, v145
	v_lshlrev_b32_e32 v104, 16, v149
	v_cndmask_b32_e64 v29, 0, v29, s[10:11]
	v_sub_f32_e32 v28, v28, v146
	v_sub_f32_e32 v97, v97, v145
	v_cndmask_b32_e64 v104, 0, v104, s[8:9]
	v_lshlrev_b32_e32 v147, 16, v153
	v_and_b32_e32 v148, 0xffff0000, v149
	s_waitcnt vmcnt(8)
	v_lshlrev_b32_e32 v170, 16, v64
	v_and_b32_e32 v64, 0xffff0000, v64
	v_cndmask_b32_e64 v64, 0, v64, s[8:9]
	v_sub_f32_e32 v172, v64, v95
	v_lshlrev_b32_e32 v64, 16, v65
	v_cndmask_b32_e64 v64, 0, v64, s[8:9]
	v_sub_f32_e32 v174, v64, v100
	v_and_b32_e32 v64, 0xffff0000, v65
	s_waitcnt vmcnt(6)
	v_and_b32_e32 v65, 0xffff0000, v69
	v_cndmask_b32_e64 v65, 0, v65, s[10:11]
	v_sub_f32_e32 v177, v65, v99
	v_lshlrev_b32_e32 v65, 16, v70
	v_cndmask_b32_e64 v65, 0, v65, s[10:11]
	v_sub_f32_e32 v179, v65, v102
	v_and_b32_e32 v65, 0xffff0000, v70
	v_cndmask_b32_e64 v65, 0, v65, s[10:11]
	v_cndmask_b32_e64 v64, 0, v64, s[8:9]
	v_sub_f32_e32 v181, v65, v101
	v_lshlrev_b32_e32 v65, 16, v71
	s_waitcnt lgkmcnt(7)
	v_fmac_f32_e32 v145, v30, v81
	v_lshlrev_b32_e32 v110, 16, v31
	v_sub_f32_e32 v29, v29, v146
	v_cndmask_b32_e64 v147, 0, v147, s[10:11]
	v_sub_f32_e32 v104, v104, v144
	v_cndmask_b32_e64 v148, 0, v148, s[8:9]
	v_and_b32_e32 v149, 0xffff0000, v153
	v_lshlrev_b32_e32 v152, 16, v150
	v_lshlrev_b32_e32 v171, 16, v68
	v_and_b32_e32 v68, 0xffff0000, v68
	v_sub_f32_e32 v176, v64, v99
	v_lshlrev_b32_e32 v64, 16, v66
	v_cndmask_b32_e64 v65, 0, v65, s[10:11]
	v_fmac_f32_e32 v146, v28, v80
	s_waitcnt lgkmcnt(5)
	v_fmac_f32_e32 v145, v97, v85
	v_sub_f32_e32 v147, v147, v144
	v_cndmask_b32_e64 v149, 0, v149, s[10:11]
	v_sub_f32_e32 v148, v148, v143
	v_cndmask_b32_e64 v152, 0, v152, s[8:9]
	v_lshlrev_b32_e32 v153, 16, v154
	v_and_b32_e32 v150, 0xffff0000, v150
	v_cndmask_b32_e64 v68, 0, v68, s[10:11]
	v_cndmask_b32_e64 v64, 0, v64, s[8:9]
	v_sub_f32_e32 v189, v65, v110
	v_fmac_f32_e32 v146, v29, v84
	v_fmac_f32_e32 v144, v104, v82
	s_waitcnt vmcnt(4)
	v_mul_f32_e32 v65, v161, v145
	v_sub_f32_e32 v149, v149, v143
	v_cndmask_b32_e64 v153, 0, v153, s[10:11]
	v_sub_f32_e32 v152, v152, v141
	v_cndmask_b32_e64 v150, 0, v150, s[8:9]
	v_and_b32_e32 v154, 0xffff0000, v154
	v_lshlrev_b32_e32 v168, 16, v151
	v_sub_f32_e32 v173, v68, v95
	v_lshlrev_b32_e32 v68, 16, v69
	v_sub_f32_e32 v178, v64, v102
	v_and_b32_e32 v64, 0xffff0000, v66
	v_fmac_f32_e32 v144, v147, v86
	v_fmac_f32_e32 v143, v148, v83
	v_mul_f32_e32 v66, v160, v146
	v_mul_f32_e32 v28, v65, v65
	v_sub_f32_e32 v153, v153, v141
	v_cndmask_b32_e64 v154, 0, v154, s[10:11]
	v_sub_f32_e32 v150, v150, v140
	v_cndmask_b32_e64 v168, 0, v168, s[8:9]
	v_lshlrev_b32_e32 v169, 16, v155
	v_and_b32_e32 v151, 0xffff0000, v151
	v_cndmask_b32_e64 v68, 0, v68, s[10:11]
	v_fmac_f32_e32 v143, v149, v87
	v_fmac_f32_e32 v141, v152, v72
	v_fmac_f32_e32 v28, v66, v66
	v_mul_f32_e32 v69, v162, v144
	v_sub_f32_e32 v154, v154, v140
	v_cndmask_b32_e64 v169, 0, v169, s[10:11]
	v_sub_f32_e32 v168, v168, v139
	v_cndmask_b32_e64 v151, 0, v151, s[8:9]
	v_and_b32_e32 v155, 0xffff0000, v155
	v_sub_f32_e32 v175, v68, v100
	s_waitcnt lgkmcnt(4)
	v_fmac_f32_e32 v141, v153, v76
	v_fmac_f32_e32 v140, v150, v73
	v_fmac_f32_e32 v28, v69, v69
	v_mul_f32_e32 v68, v163, v143
	v_sub_f32_e32 v169, v169, v139
	v_cndmask_b32_e64 v155, 0, v155, s[10:11]
	v_sub_f32_e32 v151, v151, v138
	v_cndmask_b32_e64 v64, 0, v64, s[8:9]
	v_fmac_f32_e32 v140, v154, v77
	v_fmac_f32_e32 v139, v168, v74
	v_fmac_f32_e32 v28, v68, v68
	v_mul_f32_e32 v72, v156, v141
	v_sub_f32_e32 v155, v155, v138
	v_sub_f32_e32 v180, v64, v101
	v_lshlrev_b32_e32 v64, 16, v67
	v_fmac_f32_e32 v139, v169, v78
	v_fmac_f32_e32 v138, v151, v75
	v_fmac_f32_e32 v28, v72, v72
	v_mul_f32_e32 v70, v157, v140
	v_cndmask_b32_e64 v64, 0, v64, s[8:9]
	v_fmac_f32_e32 v138, v155, v79
	v_fmac_f32_e32 v28, v70, v70
	v_mul_f32_e32 v73, v158, v139
	v_sub_f32_e32 v188, v64, v110
	v_fmac_f32_e32 v28, v73, v73
	v_mul_f32_e32 v64, v159, v138
	v_cndmask_b32_e64 v170, 0, v170, s[8:9]
	v_fmac_f32_e32 v28, v64, v64
	v_cndmask_b32_e64 v171, 0, v171, s[10:11]
	v_sub_f32_e32 v170, v170, v98
	v_add_f32_dpp v28, v28, v28 quad_perm:[1,0,3,2] row_mask:0xf bank_mask:0xf bound_ctrl:1
	v_sub_f32_e32 v171, v171, v98
	s_waitcnt lgkmcnt(3)
	v_fmac_f32_e32 v98, v170, v60
	v_fmac_f32_e32 v95, v172, v61
	v_fmac_f32_e32 v100, v174, v62
	v_fmac_f32_e32 v99, v176, v63
	s_waitcnt lgkmcnt(2)
	v_fmac_f32_e32 v102, v178, v32
	v_fmac_f32_e32 v101, v180, v33
	v_fmac_f32_e32 v110, v188, v34
	v_add_f32_dpp v62, v28, v28 quad_perm:[2,3,0,1] row_mask:0xf bank_mask:0xf bound_ctrl:1
	s_waitcnt lgkmcnt(1)
	v_fmac_f32_e32 v98, v171, v164
	v_fmac_f32_e32 v95, v173, v165
	v_mov_b32_dpp v63, v62 row_half_mirror row_mask:0xf bank_mask:0xf bound_ctrl:1
	v_fmac_f32_e32 v100, v175, v166
	v_fmac_f32_e32 v99, v177, v167
	s_waitcnt lgkmcnt(0)
	v_fmac_f32_e32 v102, v179, v88
	v_fmac_f32_e32 v101, v181, v89
	v_fmac_f32_e32 v110, v189, v90
	s_cbranch_vccnz .LBB0_393
	s_mov_b64 s[0:1], 0

.Lfp1_join:
	v_pk_add_f32 v[164:165], v[46:47], v[28:29] op_sel_hi:[1,0] neg_lo:[0,1] neg_hi:[0,1]
	v_pk_add_f32 v[174:175], v[44:45], v[36:37] op_sel_hi:[1,0] neg_lo:[0,1] neg_hi:[0,1]
	v_pk_add_f32 v[176:177], v[48:49], v[34:35] op_sel_hi:[1,0] neg_lo:[0,1] neg_hi:[0,1]
	ds_read_b128 v[44:47], v29
	ds_read_b128 v[48:51], v29 offset:256
	v_and_b32_e32 v78, 0xffff0000, v40
	v_pk_add_f32 v[150:151], v[150:151], v[78:79] op_sel_hi:[1,0] neg_lo:[0,1] neg_hi:[0,1]
	v_mul_lo_u32 v33, v142, s39
	s_waitcnt lgkmcnt(1)
	v_mov_b32_e32 v178, v44
	s_waitcnt lgkmcnt(0)
	v_mov_b32_e32 v179, v48
	v_mov_b32_e32 v48, v45
	v_pk_mul_f32 v[44:45], v[150:151], v[48:49]
	v_lshlrev_b32_e32 v80, 16, v41
	v_and_b32_e32 v82, 0xffff0000, v41
	v_lshlrev_b32_e32 v88, 16, v43
	v_add3_u32 v71, v111, v104, v33
	v_pk_add_f32 v[160:161], v[160:161], v[32:33] op_sel_hi:[1,0] neg_lo:[0,1] neg_hi:[0,1]
	v_add_f32_e32 v33, v44, v78
	v_pk_add_f32 v[152:153], v[152:153], v[80:81] op_sel_hi:[1,0] neg_lo:[0,1] neg_hi:[0,1]
	v_pk_add_f32 v[166:167], v[52:53], v[82:83] op_sel_hi:[1,0] neg_lo:[0,1] neg_hi:[0,1]
	v_pk_add_f32 v[168:169], v[56:57], v[84:85] op_sel_hi:[1,0] neg_lo:[0,1] neg_hi:[0,1]
	v_pk_add_f32 v[170:171], v[54:55], v[88:89] op_sel_hi:[1,0] neg_lo:[0,1] neg_hi:[0,1]
	v_pk_add_f32 v[172:173], v[58:59], v[60:61] op_sel_hi:[1,0] neg_lo:[0,1] neg_hi:[0,1]
	ds_read_b128 v[52:55], v29 offset:16
	ds_read_b128 v[56:59], v29 offset:272
	v_add_f32_e32 v33, v33, v45
	v_mov_b32_e32 v44, v46
	v_mov_b32_e32 v45, v50
	v_lshlrev_b32_e32 v76, 16, v40
	v_pk_mul_f32 v[44:45], v[152:153], v[44:45]
	v_pk_add_f32 v[148:149], v[148:149], v[76:77] op_sel_hi:[1,0] neg_lo:[0,1] neg_hi:[0,1]
	v_add_f32_e32 v35, v44, v80
	v_mov_b32_e32 v50, v47
	v_pk_mul_f32 v[148:149], v[148:149], v[178:179]
	v_add_f32_e32 v35, v35, v45
	v_pk_mul_f32 v[44:45], v[166:167], v[50:51]
	v_lshlrev_b32_e32 v40, 16, v37
	v_add_f32_e32 v29, v148, v76
	v_add_f32_e32 v37, v44, v82
	v_add_f32_e32 v29, v29, v149
	v_add_f32_e32 v37, v37, v45
	s_waitcnt lgkmcnt(1)
	v_mov_b32_e32 v44, v52
	s_waitcnt lgkmcnt(0)
	v_mov_b32_e32 v45, v56
	v_pk_mul_f32 v[44:45], v[168:169], v[44:45]
	v_add_f32_e32 v29, v29, v29
	v_pk_add_f32 v[154:155], v[154:155], v[86:87] op_sel_hi:[1,0] neg_lo:[0,1] neg_hi:[0,1]
	v_pk_add_f32 v[158:159], v[158:159], v[40:41] op_sel_hi:[1,0] neg_lo:[0,1] neg_hi:[0,1]
	v_add_f32_e32 v41, v44, v84
	v_mov_b32_e32 v56, v53
	v_mul_f32_e32 v29, 0x3fb8aa3b, v29
	v_add_f32_e32 v33, v33, v33
	v_add_f32_e32 v41, v41, v45
	v_pk_mul_f32 v[44:45], v[154:155], v[56:57]
	v_exp_f32_e32 v29, v29
	v_mul_f32_e32 v33, 0x3fb8aa3b, v33
	v_and_b32_e32 v90, 0xffff0000, v43
	v_pk_add_f32 v[156:157], v[156:157], v[42:43] op_sel_hi:[1,0] neg_lo:[0,1] neg_hi:[0,1]
	v_add_f32_e32 v43, v44, v86
	v_exp_f32_e32 v33, v33
	v_add_f32_e32 v43, v43, v45
	v_mov_b32_e32 v44, v54
	v_mov_b32_e32 v45, v58
	v_pk_mul_f32 v[44:45], v[170:171], v[44:45]
	v_add_f32_e32 v29, 1.0, v29
	v_add_f32_e32 v44, v44, v88
	v_add_f32_e32 v47, v44, v45
	v_rcp_f32_e32 v44, v29
	v_add_f32_e32 v29, 1.0, v33
	v_add_f32_e32 v33, v35, v35
	v_mul_f32_e32 v33, 0x3fb8aa3b, v33
	v_add_f32_e32 v35, v37, v37
	v_rcp_f32_e32 v45, v29
	v_exp_f32_e32 v33, v33
	v_mul_f32_e32 v35, 0x3fb8aa3b, v35
	v_pk_add_f32 v[38:39], v[38:39], v[90:91] op_sel_hi:[1,0] neg_lo:[0,1] neg_hi:[0,1]
	v_mov_b32_e32 v58, v55
	v_exp_f32_e32 v35, v35
	v_pk_mul_f32 v[38:39], v[38:39], v[58:59]
	v_add_f32_e32 v33, 1.0, v33
	v_add_f32_e32 v29, v38, v90
	v_add_f32_e32 v29, v29, v39
	v_pk_fma_f32 v[38:39], v[44:45], 2.0, 1.0 op_sel_hi:[1,0,0] neg_lo:[1,0,0] neg_hi:[1,0,0]
	v_add_f32_e32 v29, v29, v29
	v_cvt_pk_bf16_f32 v44, v38, v39
	v_rcp_f32_e32 v38, v33
	v_add_f32_e32 v33, 1.0, v35
	v_rcp_f32_e32 v39, v33
	v_add_f32_e32 v33, v41, v41
	v_mul_f32_e32 v33, 0x3fb8aa3b, v33
	v_add_f32_e32 v35, v43, v43
	v_exp_f32_e32 v33, v33
	v_mul_f32_e32 v35, 0x3fb8aa3b, v35
	v_exp_f32_e32 v35, v35
	v_mul_f32_e32 v29, 0x3fb8aa3b, v29
	v_add_f32_e32 v33, 1.0, v33
	v_rcp_f32_e32 v46, v33
	v_add_f32_e32 v33, 1.0, v35
	v_add_f32_e32 v35, v47, v47
	v_mul_f32_e32 v35, 0x3fb8aa3b, v35
	v_exp_f32_e32 v35, v35
	v_exp_f32_e32 v29, v29
	v_rcp_f32_e32 v47, v33
	v_pk_fma_f32 v[38:39], v[38:39], 2.0, 1.0 op_sel_hi:[1,0,0] neg_lo:[1,0,0] neg_hi:[1,0,0]
	v_add_f32_e32 v33, 1.0, v35
	v_add_f32_e32 v29, 1.0, v29
	v_rcp_f32_e32 v48, v33
	v_rcp_f32_e32 v49, v29
	v_cvt_pk_bf16_f32 v45, v38, v39
	v_pk_fma_f32 v[38:39], v[46:47], 2.0, 1.0 op_sel_hi:[1,0,0] neg_lo:[1,0,0] neg_hi:[1,0,0]
	v_add_u32_e32 v31, v118, v67
	v_cvt_pk_bf16_f32 v46, v38, v39
	v_pk_fma_f32 v[38:39], v[48:49], 2.0, 1.0 op_sel_hi:[1,0,0] neg_lo:[1,0,0] neg_hi:[1,0,0]
	s_lshl_b32 s0, s26, 10
	v_cvt_pk_bf16_f32 v47, v38, v39
	ds_write_b128 v71, v[44:47]
	ds_read_b128 v[44:47], v31
	ds_read_b128 v[48:51], v31 offset:256
	ds_read_b128 v[52:55], v31 offset:16
	ds_read_b128 v[56:59], v31 offset:272
	v_pk_add_f32 v[38:39], v[162:163], v[30:31] op_sel_hi:[1,0] neg_lo:[0,1] neg_hi:[0,1]
	s_or_b32 s28, s0, s5
	s_waitcnt lgkmcnt(3)
	v_mov_b32_e32 v76, v44
	s_waitcnt lgkmcnt(2)
	v_mov_b32_e32 v77, v48
	v_mov_b32_e32 v48, v45
	v_pk_mul_f32 v[44:45], v[156:157], v[48:49]
	v_mov_b32_e32 v43, v50
	v_add_f32_e32 v31, v44, v42
	v_mov_b32_e32 v42, v46
	v_pk_mul_f32 v[42:43], v[158:159], v[42:43]
	v_mov_b32_e32 v50, v47
	v_add_f32_e32 v44, v31, v45
	v_add_f32_e32 v31, v42, v40
	v_pk_mul_f32 v[40:41], v[174:175], v[50:51]
	v_add_f32_e32 v42, v31, v43
	v_add_f32_e32 v31, v40, v36
	s_waitcnt lgkmcnt(1)
	v_mov_b32_e32 v36, v52
	s_waitcnt lgkmcnt(0)
	v_mov_b32_e32 v37, v56
	v_pk_mul_f32 v[36:37], v[176:177], v[36:37]
	v_mov_b32_e32 v56, v53
	v_add_f32_e32 v40, v31, v41
	v_add_f32_e32 v31, v36, v34
	v_pk_mul_f32 v[34:35], v[160:161], v[56:57]
	v_add_f32_e32 v36, v31, v37
	v_add_f32_e32 v31, v34, v32
	v_mov_b32_e32 v32, v54
	v_mov_b32_e32 v33, v58
	v_pk_mul_f32 v[32:33], v[38:39], v[32:33]
	v_mov_b32_e32 v58, v55
	v_add_f32_e32 v30, v32, v30
	v_pk_mul_f32 v[76:77], v[172:173], v[76:77]
	v_add_f32_e32 v34, v31, v35
	v_add_f32_e32 v32, v30, v33
	v_pk_mul_f32 v[30:31], v[164:165], v[58:59]
	v_add_f32_e32 v29, v76, v60
	v_add_f32_e32 v28, v30, v28
	v_add_f32_e32 v29, v29, v77
	v_add_f32_e32 v31, v28, v31
	v_cvt_pk_bf16_f32 v28, v29, v44
	v_cvt_pk_bf16_f32 v29, v42, v40
	v_cvt_pk_bf16_f32 v30, v36, v34
	v_cvt_pk_bf16_f32 v31, v32, v31
	s_or_b32 s0, s41, s28
	s_mov_b32 s1, s29
	ds_write_b128 v71, v[28:31] offset:9216
	s_lshl_b64 s[0:1], s[0:1], 7
	v_and_b32_e32 v51, 15, v103
	v_lshrrev_b32_e32 v28, 1, v103
	s_add_u32 s60, s51, s0
	v_and_b32_e32 v50, 24, v28
	v_or_b32_e32 v48, s27, v51
	s_addc_u32 s61, s70, s1
	v_lshlrev_b32_e32 v44, 1, v50
	v_mov_b32_e32 v45, v105
	v_ashrrev_i32_e32 v49, 31, v48
	v_lshl_add_u64 v[28:29], s[60:61], 0, v[44:45]
	v_lshlrev_b64 v[30:31], 7, v[48:49]
	v_lshl_add_u64 v[32:33], v[28:29], 0, v[30:31]
	global_load_dwordx4 v[52:55], v[32:33], off
	global_load_dwordx4 v[56:59], v[32:33], off offset:64
	v_or_b32_e32 v49, s41, v51
	v_add_u32_e32 v32, s27, v49
	v_ashrrev_i32_e32 v33, 31, v32
	v_lshl_add_u64 v[32:33], v[32:33], 0, s[28:29]
	v_readlane_b32 s76, v253, 26
	v_lshlrev_b64 v[32:33], 2, v[32:33]
	v_readlane_b32 s90, v253, 40
	v_readlane_b32 s91, v253, 41
	s_add_u32 s0, s71, s0
	s_addc_u32 s1, s49, s1
	v_lshl_add_u64 v[34:35], s[90:91], 0, v[32:33]
	global_load_dword v60, v[34:35], off
	v_lshl_add_u64 v[34:35], s[0:1], 0, v[44:45]
	v_lshl_add_u64 v[30:31], v[34:35], 0, v[30:31]
	global_load_dwordx4 v[76:79], v[30:31], off
	global_load_dwordx4 v[80:83], v[30:31], off offset:64
	v_readlane_b32 s77, v253, 27
	v_readlane_b32 s78, v253, 28
	v_readlane_b32 s79, v253, 29
	v_readlane_b32 s80, v253, 30
	v_readlane_b32 s81, v253, 31
	v_readlane_b32 s82, v253, 32
	v_readlane_b32 s83, v253, 33
	v_readlane_b32 s84, v253, 34
	v_readlane_b32 s85, v253, 35
	v_readlane_b32 s86, v253, 36
	v_readlane_b32 s87, v253, 37
	v_readlane_b32 s72, v253, 42
	v_readlane_b32 s74, v253, 44
	v_readlane_b32 s75, v253, 45
	v_or_b32_e32 v46, s63, v51
	v_ashrrev_i32_e32 v47, 31, v46
	v_lshl_add_u64 v[30:31], s[74:75], 0, v[32:33]
	global_load_dword v71, v[30:31], off
	v_lshlrev_b64 v[30:31], 7, v[46:47]
	v_lshl_add_u64 v[28:29], v[28:29], 0, v[30:31]
	v_lshl_add_u64 v[30:31], v[34:35], 0, v[30:31]
	global_load_dwordx4 v[84:87], v[28:29], off
	global_load_dwordx4 v[88:91], v[28:29], off offset:64
	global_load_dwordx4 v[148:151], v[30:31], off
	global_load_dwordx4 v[152:155], v[30:31], off offset:64
	v_add_u32_e32 v156, s63, v49
	s_lshl_b32 s41, s41, 2
	v_ashrrev_i32_e32 v157, 31, v156
	v_or_b32_e32 v45, s34, v51
	s_add_u32 s0, s42, s41
	v_lshl_add_u64 v[156:157], v[156:157], 0, s[28:29]
	v_mul_u32_u24_e32 v45, 0x48, v45
	s_addc_u32 s1, s36, 0
	v_lshlrev_b64 v[156:157], 2, v[156:157]
	v_lshlrev_b32_e32 v45, 1, v45
	s_add_u32 s60, s52, s41
	v_lshl_add_u64 v[158:159], s[90:91], 0, v[156:157]
	v_lshl_add_u64 v[156:157], s[74:75], 0, v[156:157]
	v_add3_u32 v45, v111, v45, v44
	s_addc_u32 s61, s53, 0
	global_load_dwordx4 v[32:35], v67, s[0:1] offset:16
	global_load_dwordx4 v[40:43], v67, s[0:1]
	global_load_dwordx4 v[28:31], v67, s[60:61] offset:16
	global_load_dwordx4 v[36:39], v67, s[60:61]
	global_load_dword v75, v[156:157], off
	s_mov_b32 s0, 0xbfb8aa3b
	global_load_dword v67, v[158:159], off
	s_waitcnt lgkmcnt(0)
	s_barrier
	ds_read_b128 v[156:159], v45
	ds_read_b128 v[160:163], v45 offset:64
	s_waitcnt vmcnt(15) lgkmcnt(1)
	v_mfma_f32_16x16x32_bf16 v[52:55], v[156:159], v[52:55], 0
	ds_read_b128 v[164:167], v45 offset:9216
	s_movk_i32 s1, 0x41
	v_and_b32_e32 v49, 63, v103
	s_waitcnt vmcnt(14) lgkmcnt(1)
	v_mfma_f32_16x16x32_bf16 v[52:55], v[160:163], v[56:59], v[52:55]
	v_readlane_b32 s88, v253, 38
	v_readlane_b32 s89, v253, 39
	v_readlane_b32 s73, v253, 43
	v_readlane_b32 s76, v253, 46
	v_readlane_b32 s77, v253, 47
	v_readlane_b32 s78, v253, 48
	v_readlane_b32 s79, v253, 49
	v_readlane_b32 s80, v253, 50
	s_waitcnt vmcnt(13)
	v_add_f32_e32 v52, v60, v52
	v_mul_f32_e64 v47, |v52|, s0
	v_exp_f32_e32 v56, v47
	v_lshrrev_b32_e32 v47, 2, v103
	v_add_f32_e32 v53, v60, v53
	v_add_f32_e32 v54, v60, v54
	v_add_f32_e32 v56, 1.0, v56
	v_log_f32_e32 v147, v56
	ds_read_b128 v[56:59], v45 offset:9280
	s_waitcnt vmcnt(12) lgkmcnt(1)
	v_mfma_f32_16x16x32_bf16 v[76:79], v[164:167], v[76:79], 0
	v_max_f32_e64 v45, -v52, 0
	v_fmac_f32_e32 v45, 0x3f317218, v147
	v_sub_f32_e32 v45, -0.5, v45
	s_waitcnt vmcnt(11) lgkmcnt(0)
	v_mfma_f32_16x16x32_bf16 v[76:79], v[56:59], v[80:83], v[76:79]
	v_mul_f32_e32 v45, 0x3fb8aa3b, v45
	v_exp_f32_e32 v52, v45
	v_and_b32_e32 v45, 12, v47
	s_waitcnt vmcnt(10)
	s_nop 3
	v_add_f32_e32 v76, v71, v76
	v_mul_f32_e32 v76, 0xbfb8aa3b, v76
	v_exp_f32_e32 v76, v76
	v_or_b32_e32 v147, s34, v45
	v_mul_u32_u24_e32 v80, 0x41, v147
	v_add_lshl_u32 v81, v80, v48, 2
	v_add_f32_e32 v76, 1.0, v76
	v_rcp_f32_e32 v76, v76
	v_mul_f32_e64 v82, |v53|, s0
	v_xor_b32_e32 v52, 0x80000000, v52
	v_exp_f32_e32 v82, v82
	v_add_u32_e32 v83, v113, v81
	ds_write_b32 v83, v52
	v_add_u32_e32 v52, v119, v81
	ds_write_b32 v52, v76
	v_add_f32_e32 v76, v71, v77
	v_mul_f32_e64 v77, |v54|, s0
	v_exp_f32_e32 v77, v77
	v_add_f32_e32 v82, 1.0, v82
	v_log_f32_e32 v82, v82
	v_max_f32_e64 v53, -v53, 0
	v_add_f32_e32 v77, 1.0, v77
	v_log_f32_e32 v77, v77
	v_fmac_f32_e32 v53, 0x3f317218, v82
	v_mul_f32_e32 v76, 0xbfb8aa3b, v76
	v_sub_f32_e32 v53, -0.5, v53
	v_exp_f32_e32 v76, v76
	v_mul_f32_e32 v53, 0x3fb8aa3b, v53
	v_max_f32_e64 v54, -v54, 0
	v_exp_f32_e32 v53, v53
	v_fmac_f32_e32 v54, 0x3f317218, v77
	v_sub_f32_e32 v54, -0.5, v54
	v_add_f32_e32 v55, v60, v55
	v_add_f32_e32 v76, 1.0, v76
	v_mul_f32_e32 v54, 0x3fb8aa3b, v54
	v_mul_f32_e64 v60, |v55|, s0
	v_mad_u32_u24 v81, v147, s1, s1
	v_rcp_f32_e32 v76, v76
	v_exp_f32_e32 v54, v54
	v_exp_f32_e32 v60, v60
	v_xor_b32_e32 v52, 0x80000000, v53
	v_add_lshl_u32 v53, v81, v48, 2
	v_add_u32_e32 v82, v113, v53
	ds_write_b32 v82, v52
	v_add_u32_e32 v52, v119, v53
	ds_write_b32 v52, v76
	v_xor_b32_e32 v52, 0x80000000, v54
	v_add_f32_e32 v54, v71, v78
	v_add_f32_e32 v60, 1.0, v60
	v_mul_f32_e32 v54, 0xbfb8aa3b, v54
	v_log_f32_e32 v60, v60
	v_exp_f32_e32 v54, v54
	v_max_f32_e64 v55, -v55, 0
	v_mov_b32_e32 v53, 0x82
	v_fmac_f32_e32 v55, 0x3f317218, v60
	v_add_f32_e32 v54, 1.0, v54
	v_sub_f32_e32 v55, -0.5, v55
	v_mad_u32_u24 v82, v147, s1, v53
	v_rcp_f32_e32 v54, v54
	v_mul_f32_e32 v55, 0x3fb8aa3b, v55
	v_add_lshl_u32 v53, v82, v48, 2
	v_exp_f32_e32 v55, v55
	v_add_u32_e32 v76, v113, v53
	ds_write_b32 v76, v52
	v_add_u32_e32 v52, v119, v53
	ds_write_b32 v52, v54
	v_mov_b32_e32 v52, 0xc3
	v_xor_b32_e32 v60, 0x80000000, v55
	v_mad_u32_u24 v83, v147, s1, v52
	s_waitcnt vmcnt(9)
	v_mfma_f32_16x16x32_bf16 v[52:55], v[156:159], v[84:87], 0
	v_add_f32_e32 v71, v71, v79
	v_mul_f32_e32 v71, 0xbfb8aa3b, v71
	v_exp_f32_e32 v71, v71
	s_waitcnt vmcnt(8)
	v_mfma_f32_16x16x32_bf16 v[52:55], v[160:163], v[88:91], v[52:55]
	v_add_lshl_u32 v48, v83, v48, 2
	v_add_u32_e32 v76, v113, v48
	ds_write_b32 v76, v60
	v_add_f32_e32 v60, 1.0, v71
	v_rcp_f32_e32 v60, v60
	s_waitcnt vmcnt(0)
	s_nop 1
	v_add_f32_e32 v52, v67, v52
	v_mul_f32_e64 v77, |v52|, s0
	v_exp_f32_e32 v77, v77
	v_add_u32_e32 v48, v119, v48
	v_add_f32_e32 v53, v67, v53
	v_max_f32_e64 v52, -v52, 0
	v_add_f32_e32 v71, 1.0, v77
	v_mfma_f32_16x16x32_bf16 v[76:79], v[164:167], v[148:151], 0
	v_log_f32_e32 v71, v71
	ds_write_b32 v48, v60
	v_mul_f32_e64 v60, |v53|, s0
	v_mfma_f32_16x16x32_bf16 v[56:59], v[56:59], v[152:155], v[76:79]
	v_fmac_f32_e32 v52, 0x3f317218, v71
	v_exp_f32_e32 v60, v60
	v_sub_f32_e32 v52, -0.5, v52
	v_mul_f32_e32 v52, 0x3fb8aa3b, v52
	v_exp_f32_e32 v52, v52
	s_nop 2
	v_add_f32_e32 v56, v75, v56
	v_mul_f32_e32 v56, 0xbfb8aa3b, v56
	v_exp_f32_e32 v56, v56
	v_add_f32_e32 v60, 1.0, v60
	v_log_f32_e32 v60, v60
	v_xor_b32_e32 v48, 0x80000000, v52
	v_add_f32_e32 v56, 1.0, v56
	v_rcp_f32_e32 v56, v56
	v_add_lshl_u32 v52, v80, v46, 2
	v_add_u32_e32 v71, v113, v52
	v_max_f32_e64 v53, -v53, 0
	v_fmac_f32_e32 v53, 0x3f317218, v60
	ds_write_b32 v71, v48
	v_add_u32_e32 v48, v119, v52
	v_add_f32_e32 v54, v67, v54
	v_sub_f32_e32 v53, -0.5, v53
	ds_write_b32 v48, v56
	v_mul_f32_e64 v56, |v54|, s0
	v_mul_f32_e32 v53, 0x3fb8aa3b, v53
	v_exp_f32_e32 v56, v56
	v_exp_f32_e32 v53, v53
	v_max_f32_e64 v54, -v54, 0
	v_add_lshl_u32 v52, v81, v46, 2
	v_add_f32_e32 v56, 1.0, v56
	v_xor_b32_e32 v48, 0x80000000, v53
	v_add_f32_e32 v53, v75, v57
	v_log_f32_e32 v56, v56
	v_mul_f32_e32 v53, 0xbfb8aa3b, v53
	v_exp_f32_e32 v53, v53
	v_add_u32_e32 v57, v113, v52
	v_fmac_f32_e32 v54, 0x3f317218, v56
	v_sub_f32_e32 v54, -0.5, v54
	v_add_f32_e32 v53, 1.0, v53
	v_mul_f32_e32 v54, 0x3fb8aa3b, v54
	v_rcp_f32_e32 v53, v53
	v_exp_f32_e32 v54, v54
	ds_write_b32 v57, v48
	v_add_u32_e32 v48, v119, v52
	ds_write_b32 v48, v53
	v_xor_b32_e32 v48, 0x80000000, v54
	v_add_f32_e32 v53, v75, v58
	v_add_f32_e32 v54, v67, v55
	v_mul_f32_e32 v53, 0xbfb8aa3b, v53
	v_mul_f32_e64 v55, |v54|, s0
	v_exp_f32_e32 v53, v53
	v_exp_f32_e32 v55, v55
	v_add_lshl_u32 v52, v82, v46, 2
	v_add_u32_e32 v56, v113, v52
	ds_write_b32 v56, v48
	v_add_f32_e32 v48, 1.0, v53
	v_add_f32_e32 v53, 1.0, v55
	v_log_f32_e32 v53, v53
	v_max_f32_e64 v54, -v54, 0
	v_rcp_f32_e32 v48, v48
	v_add_u32_e32 v52, v119, v52
	v_fmac_f32_e32 v54, 0x3f317218, v53
	v_sub_f32_e32 v53, -0.5, v54
	v_mul_f32_e32 v53, 0x3fb8aa3b, v53
	v_exp_f32_e32 v53, v53
	v_add_f32_e32 v54, v75, v59
	v_mul_f32_e32 v54, 0xbfb8aa3b, v54
	v_add_lshl_u32 v46, v83, v46, 2
	v_exp_f32_e32 v54, v54
	ds_write_b32 v52, v48
	v_xor_b32_e32 v48, 0x80000000, v53
	v_add_u32_e32 v53, v113, v46
	ds_write_b32 v53, v48
	v_ashrrev_i32_e32 v48, 6, v103
	v_lshlrev_b32_e32 v59, 3, v48
	v_or_b32_e32 v53, 1, v59
	v_add_f32_e32 v52, 1.0, v54
	v_sub_u32_e32 v54, 63, v53
	v_cndmask_b32_e64 v53, v54, v53, s[12:13]
	v_or_b32_e32 v54, 2, v59
	v_sub_u32_e32 v55, 63, v54
	v_cndmask_b32_e64 v54, v55, v54, s[12:13]
	v_or_b32_e32 v55, 3, v59
	v_sub_u32_e32 v56, 63, v55
	v_rcp_f32_e32 v52, v52
	v_cndmask_b32_e64 v55, v56, v55, s[12:13]
	v_or_b32_e32 v56, 4, v59
	v_sub_u32_e32 v57, 63, v56
	v_cndmask_b32_e64 v56, v57, v56, s[12:13]
	v_or_b32_e32 v57, 5, v59
	v_add_u32_e32 v46, v119, v46
	v_sub_u32_e32 v58, 63, v57
	ds_write_b32 v46, v52
	v_sub_u32_e32 v52, 63, v59
	v_cndmask_b32_e64 v57, v58, v57, s[12:13]
	v_or_b32_e32 v58, 6, v59
	v_cndmask_b32_e64 v52, v52, v59, s[12:13]
	v_sub_u32_e32 v67, 63, v58
	v_or_b32_e32 v59, 7, v59
	v_lshlrev_b32_e32 v46, 2, v49
	s_movk_i32 s0, 0x104
	v_cndmask_b32_e64 v58, v67, v58, s[12:13]
	v_sub_u32_e32 v67, 63, v59
	v_add_u32_e32 v60, v113, v46
	v_mul_lo_u32 v52, v52, s0
	v_cndmask_b32_e64 v59, v67, v59, s[12:13]
	v_add_u32_e32 v52, v60, v52
	v_mul_lo_u32 v53, v53, s0
	v_mul_lo_u32 v54, v54, s0
	v_mul_lo_u32 v55, v55, s0
	v_mul_lo_u32 v56, v56, s0
	v_mul_lo_u32 v57, v57, s0
	v_mul_lo_u32 v58, v58, s0
	v_mul_lo_u32 v59, v59, s0
	s_waitcnt lgkmcnt(0)
	s_barrier
	v_add_u32_e32 v53, v60, v53
	v_add_u32_e32 v54, v60, v54
	v_add_u32_e32 v55, v60, v55
	v_add_u32_e32 v56, v60, v56
	v_add_u32_e32 v57, v60, v57
	v_add_u32_e32 v58, v60, v58
	v_add_u32_e32 v59, v60, v59
	ds_read_b32 v60, v52
	ds_read_b32 v67, v53
	ds_read_b32 v71, v54
	ds_read_b32 v75, v55
	ds_read_b32 v80, v56
	ds_read_b32 v81, v57
	ds_read_b32 v82, v58
	ds_read_b32 v83, v59
	s_waitcnt lgkmcnt(7)
	v_add_f32_e32 v79, 0, v60
	s_waitcnt lgkmcnt(6)
	v_add_f32_e32 v78, v79, v67
	s_waitcnt lgkmcnt(5)
	v_add_f32_e32 v77, v78, v71
	s_waitcnt lgkmcnt(4)
	v_add_f32_e32 v76, v77, v75
	s_waitcnt lgkmcnt(3)
	v_add_f32_e32 v75, v76, v80
	s_waitcnt lgkmcnt(2)
	v_add_f32_e32 v71, v75, v81
	s_waitcnt lgkmcnt(1)
	v_add_f32_e32 v67, v71, v82
	s_waitcnt lgkmcnt(0)
	v_add_f32_e32 v60, v67, v83
	v_lshl_add_u32 v80, v103, 2, v120
	ds_write_b32 v80, v60
	v_add_u32_e32 v81, v120, v46
	v_cmp_lt_i32_e32 vcc, 0, v48
	v_mov_b32_e32 v80, 0
	v_readlane_b32 s81, v253, 51
	v_readlane_b32 s82, v253, 52
	v_readlane_b32 s83, v253, 53
	v_readlane_b32 s84, v253, 54
	v_readlane_b32 s85, v253, 55
	v_readlane_b32 s86, v253, 56
	v_readlane_b32 s87, v253, 57
	s_waitcnt lgkmcnt(0)
	s_barrier
	ds_read_b32 v216, v81
	ds_read_b32 v217, v81 offset:256
	ds_read_b32 v218, v81 offset:512
	ds_read_b32 v219, v81 offset:768
	ds_read_b32 v220, v81 offset:1024
	ds_read_b32 v221, v81 offset:1280
	ds_read_b32 v222, v81 offset:1536
	v_readfirstlane_b32 s0, v48
	s_movk_i32 s75, 0xfc0
	s_waitcnt lgkmcnt(0)
	s_cmp_lt_i32 s0, 1
	s_cbranch_scc1 .Lseg_done
	v_add_f32_e32 v80, 0, v216
	s_cmp_lt_i32 s0, 2
	s_cbranch_scc1 .Lseg_done
	v_add_f32_e32 v80, v80, v217
	s_cmp_lt_i32 s0, 3
	s_cbranch_scc1 .Lseg_done
	v_add_f32_e32 v80, v80, v218
	s_cmp_lt_i32 s0, 4
	s_cbranch_scc1 .Lseg_done
	v_add_f32_e32 v80, v80, v219
	s_cmp_lt_i32 s0, 5
	s_cbranch_scc1 .Lseg_done
	v_add_f32_e32 v80, v80, v220
	s_cmp_lt_i32 s0, 6
	s_cbranch_scc1 .Lseg_done
	v_add_f32_e32 v80, v80, v221
	s_cmp_lt_i32 s0, 7
	s_cbranch_scc1 .Lseg_done
	v_add_f32_e32 v80, v80, v222

.LBB0_408:
	s_or_b64 exec, exec, s[0:1]
	v_lshl_add_u32 v52, v142, 6, v142
	v_lshl_add_u32 v55, v74, 2, v113
	v_lshl_add_u32 v60, v52, 2, v55
	s_waitcnt lgkmcnt(0)
	s_barrier
	s_and_b64 s[0:1], exec, s[12:13]
	ds_read_b32 v54, v60
	s_cselect_b32 s0, -1, 1
	v_sub_u32_e32 v48, 63, v142
	v_add_u32_e32 v53, s0, v142
	s_movk_i32 s0, 0x104
	v_cndmask_b32_e64 v48, v48, v142, s[12:13]
	v_mul_lo_u32 v56, v53, s0
	v_cmp_lt_i32_e32 vcc, 0, v48
	v_mov_b32_e32 v53, 0
	v_add_u32_e32 v87, v55, v56
	v_mov_b32_e32 v56, 0
	v_mov_b32_e32 v224, 0x3fb8aa3b
	v_cndmask_b32_e32 v87, v60, v87, vcc
	v_cndmask_b32_e32 v224, 0, v224, vcc
	ds_read_b32 v216, v87
	ds_read_b32 v217, v87 offset:4
	ds_read_b32 v218, v87 offset:8
	ds_read_b32 v219, v87 offset:12
	ds_read_b32 v220, v87 offset:16
	ds_read_b32 v221, v87 offset:20
	ds_read_b32 v222, v87 offset:24
	ds_read_b32 v223, v87 offset:28
	v_add_u32_e32 v52, v52, v74
	v_lshl_add_u32 v52, v52, 2, v119
	ds_read_b32 v57, v52
	ds_read_b32 v55, v60 offset:4
	ds_read_b32 v58, v52 offset:4
	ds_read_b32 v71, v60 offset:8
	ds_read_b32 v76, v52 offset:8
	ds_read_b32 v74, v60 offset:12
	s_waitcnt lgkmcnt(6)
	v_mul_f32_e32 v56, v224, v216
	v_mul_f32_e32 v53, v224, v217
	v_mul_f32_e32 v75, v224, v218
	v_mul_f32_e32 v67, v224, v219
	v_mul_f32_e32 v81, v224, v220
	v_mul_f32_e32 v78, v224, v221
	v_mul_f32_e32 v85, v224, v222
	v_mul_f32_e32 v59, v224, v223
	ds_read_b32 v77, v52 offset:12
	ds_read_b32 v79, v60 offset:16
	ds_read_b32 v82, v52 offset:16
	ds_read_b32 v80, v60 offset:20
	ds_read_b32 v83, v52 offset:20
	ds_read_b32 v84, v60 offset:24
	ds_read_b32 v86, v52 offset:24
	ds_read_b32 v60, v60 offset:28
	v_lshlrev_b32_e32 v88, 16, v16
	v_lshlrev_b32_e32 v87, 16, v8
	s_and_b64 s[100:101], s[8:9], s[10:11]
	s_cmp_eq_u64 s[100:101], exec
	s_cbranch_scc1 .Lfp3
	v_cndmask_b32_e64 v88, 0, v88, s[8:9]
	v_lshlrev_b32_e32 v89, 16, v12
	v_cndmask_b32_e64 v89, 0, v89, s[10:11]
	v_sub_f32_e32 v88, v88, v87
	v_and_b32_e32 v16, 0xffff0000, v16
	v_sub_f32_e32 v89, v89, v87
	v_fmac_f32_e32 v87, v88, v20
	v_add_f32_e32 v20, v62, v63
	v_and_b32_e32 v8, 0xffff0000, v8
	v_cndmask_b32_e64 v16, 0, v16, s[8:9]
	v_and_b32_e32 v12, 0xffff0000, v12
	v_max_f32_e32 v20, 0x179abe15, v20
	v_cndmask_b32_e64 v12, 0, v12, s[10:11]
	v_sub_f32_e32 v16, v16, v8
	v_fmac_f32_e32 v87, v89, v24
	v_rsq_f32_e32 v24, v20
	s_waitcnt lgkmcnt(13)
	v_add_f32_e32 v20, -1.0, v57
	v_sub_f32_e32 v12, v12, v8
	v_fmac_f32_e32 v8, v16, v21
	v_fma_f32 v20, v40, v20, 1.0
	v_fmac_f32_e32 v8, v12, v25
	s_waitcnt lgkmcnt(11)
	v_add_f32_e32 v12, -1.0, v58
	v_mul_f32_e32 v20, v146, v20
	v_fma_f32 v12, v41, v12, 1.0
	v_mul_f32_e32 v40, v87, v20
	v_mul_f32_e32 v12, v145, v12
	v_fma_f32 v36, v36, v40, 0
	v_mul_f32_e32 v16, v8, v12
	v_lshlrev_b32_e32 v21, 16, v17
	v_and_b32_e32 v17, 0xffff0000, v17
	v_fmac_f32_e32 v36, v37, v16
	v_lshlrev_b32_e32 v16, 16, v9
	v_cndmask_b32_e64 v21, 0, v21, s[8:9]
	v_lshlrev_b32_e32 v25, 16, v13
	v_and_b32_e32 v9, 0xffff0000, v9
	v_cndmask_b32_e64 v17, 0, v17, s[8:9]
	v_and_b32_e32 v13, 0xffff0000, v13
	v_cndmask_b32_e64 v25, 0, v25, s[10:11]
	v_sub_f32_e32 v21, v21, v16
	v_cndmask_b32_e64 v13, 0, v13, s[10:11]
	v_sub_f32_e32 v17, v17, v9
	v_sub_f32_e32 v25, v25, v16
	v_fmac_f32_e32 v16, v21, v22
	s_waitcnt lgkmcnt(9)
	v_add_f32_e32 v21, -1.0, v76
	v_sub_f32_e32 v13, v13, v9
	v_fmac_f32_e32 v9, v17, v23
	v_fma_f32 v21, v42, v21, 1.0
	v_fmac_f32_e32 v9, v13, v27
	s_waitcnt lgkmcnt(7)
	v_add_f32_e32 v13, -1.0, v77
	v_fmac_f32_e32 v16, v25, v26
	v_mul_f32_e32 v21, v144, v21
	v_fma_f32 v13, v43, v13, 1.0
	v_mul_f32_e32 v22, v16, v21
	v_mul_f32_e32 v13, v143, v13
	v_fmac_f32_e32 v36, v38, v22
	v_mul_f32_e32 v17, v9, v13
	v_lshlrev_b32_e32 v22, 16, v18
	v_fmac_f32_e32 v36, v39, v17
	v_lshlrev_b32_e32 v17, 16, v10
	v_cndmask_b32_e64 v22, 0, v22, s[8:9]
	v_lshlrev_b32_e32 v23, 16, v14
	v_cndmask_b32_e64 v23, 0, v23, s[10:11]
	v_sub_f32_e32 v22, v22, v17
	v_sub_f32_e32 v23, v23, v17
	v_fmac_f32_e32 v17, v22, v0
	s_waitcnt lgkmcnt(5)
	v_add_f32_e32 v0, -1.0, v82
	v_fma_f32 v0, v32, v0, 1.0
	v_fmac_f32_e32 v17, v23, v4
	v_mul_f32_e32 v0, v141, v0
	v_mul_f32_e32 v4, v17, v0
	v_fmac_f32_e32 v36, v28, v4
	v_and_b32_e32 v4, 0xffff0000, v10
	v_and_b32_e32 v10, 0xffff0000, v18
	v_cndmask_b32_e64 v10, 0, v10, s[8:9]
	v_and_b32_e32 v14, 0xffff0000, v14
	v_cndmask_b32_e64 v14, 0, v14, s[10:11]
	v_sub_f32_e32 v10, v10, v4
	v_sub_f32_e32 v14, v14, v4
	v_fmac_f32_e32 v4, v10, v1
	s_waitcnt lgkmcnt(3)
	v_add_f32_e32 v1, -1.0, v83
	v_fma_f32 v1, v33, v1, 1.0
	v_fmac_f32_e32 v4, v14, v5
	v_mul_f32_e32 v1, v140, v1
	v_mul_f32_e32 v5, v4, v1
	v_lshlrev_b32_e32 v10, 16, v19
	v_fmac_f32_e32 v36, v29, v5
	v_lshlrev_b32_e32 v5, 16, v11
	v_cndmask_b32_e64 v10, 0, v10, s[8:9]
	v_lshlrev_b32_e32 v14, 16, v15
	v_cndmask_b32_e64 v14, 0, v14, s[10:11]
	v_sub_f32_e32 v10, v10, v5
	v_sub_f32_e32 v14, v14, v5
	v_fmac_f32_e32 v5, v10, v2
	v_fmac_f32_e32 v5, v14, v6
	s_waitcnt lgkmcnt(2)
	v_mul_f32_e32 v10, 0x3fb8aa3b, v84
	v_exp_f32_e32 v14, v85
	v_mul_f32_e32 v18, 0xbfb8aa3b, v84
	v_exp_f32_e32 v18, v18
	v_exp_f32_e32 v10, v10
	s_waitcnt lgkmcnt(1)
	v_add_f32_e32 v6, -1.0, v86
	v_mul_f32_e32 v2, v73, v24
	v_fma_f32 v6, v34, v6, 1.0
	v_mul_f32_e32 v6, v139, v6
	v_mul_f32_e64 v25, v14, -v2
	v_mul_f32_e32 v2, v2, v86
	v_mul_f32_e32 v26, v18, v2
	v_mul_f32_e32 v18, v18, v6
	v_mul_f32_e32 v27, v5, v10
	v_mul_f32_e32 v2, v5, v6
	v_mul_f32_e32 v5, 0x3fb8aa3b, v79
	v_exp_f32_e32 v6, v81
	v_mul_f32_e32 v10, 0xbfb8aa3b, v79
	v_exp_f32_e32 v10, v10
	v_exp_f32_e32 v5, v5
	v_fmac_f32_e32 v36, v30, v2
	v_mul_f32_e32 v2, v72, v24
	v_mul_f32_e64 v6, v6, -v2
	v_mul_f32_e32 v2, v2, v82
	v_mul_f32_e32 v14, v10, v2
	v_mul_f32_e32 v0, v10, v0
	v_mul_f32_e32 v5, v17, v5
	v_mul_f32_e32 v10, 0x3fb8aa3b, v80
	v_exp_f32_e32 v17, v78
	v_mul_f32_e32 v22, 0xbfb8aa3b, v80
	v_exp_f32_e32 v22, v22
	v_exp_f32_e32 v10, v10
	v_mul_f32_e32 v2, v70, v24
	v_mul_f32_e64 v17, v17, -v2
	v_mul_f32_e32 v2, v2, v83
	v_mul_f32_e32 v23, v22, v2
	v_mul_f32_e32 v4, v4, v10
	v_cvt_pk_bf16_f32 v2, v6, v17
	v_cvt_pk_bf16_f32 v6, v14, v23
	v_cvt_pk_bf16_f32 v14, v5, v4
	v_exp_f32_e32 v4, v75
	v_mul_f32_e32 v5, 0xbfb8aa3b, v71
	v_exp_f32_e32 v5, v5
	v_mul_f32_e32 v1, v22, v1
	v_cvt_pk_bf16_f32 v10, v0, v1
	v_mul_f32_e32 v0, v69, v24
	v_mul_f32_e32 v1, 0x3fb8aa3b, v71
	v_exp_f32_e32 v1, v1
	v_mul_f32_e64 v4, v4, -v0
	v_mul_f32_e32 v0, v0, v76
	v_mul_f32_e32 v0, v5, v0
	v_mul_f32_e32 v17, v5, v21
	v_mul_f32_e32 v5, 0x3fb8aa3b, v74
	v_exp_f32_e32 v21, v67
	v_mul_f32_e32 v22, 0xbfb8aa3b, v74
	v_exp_f32_e32 v22, v22
	v_exp_f32_e32 v5, v5
	v_mul_f32_e32 v16, v16, v1
	v_mul_f32_e32 v1, v68, v24
	v_mul_f32_e64 v21, v21, -v1
	v_mul_f32_e32 v1, v1, v77
	v_mul_f32_e32 v23, v22, v1
	v_mul_f32_e32 v13, v22, v13
	v_mul_f32_e32 v22, v9, v5
	v_cvt_pk_bf16_f32 v1, v4, v21
	v_cvt_pk_bf16_f32 v9, v17, v13
	v_cvt_pk_bf16_f32 v13, v16, v22
	v_mul_f32_e32 v4, 0x3fb8aa3b, v54
	v_exp_f32_e32 v16, v56
	v_mul_f32_e32 v17, 0xbfb8aa3b, v54
	v_exp_f32_e32 v17, v17
	v_exp_f32_e32 v4, v4
	v_cvt_pk_bf16_f32 v5, v0, v23
	v_mul_f32_e32 v0, v66, v24
	v_mul_f32_e64 v16, v16, -v0
	v_mul_f32_e32 v0, v0, v57
	v_mul_f32_e32 v23, 0xbfb8aa3b, v55
	v_mul_f32_e32 v21, v17, v0
	v_mul_f32_e32 v17, v17, v20
	v_mul_f32_e32 v20, v87, v4
	v_mul_f32_e32 v4, 0x3fb8aa3b, v55
	v_exp_f32_e32 v22, v53
	v_exp_f32_e32 v23, v23
	v_exp_f32_e32 v4, v4
	v_mul_f32_e32 v0, v65, v24
	v_mul_f32_e64 v22, v22, -v0
	v_mul_f32_e32 v0, v0, v58
	v_mul_f32_e32 v12, v23, v12
	v_mul_f32_e32 v28, v23, v0
	v_mul_f32_e32 v23, v8, v4
	v_cvt_pk_bf16_f32 v0, v16, v22
	v_cvt_pk_bf16_f32 v8, v17, v12
	v_and_b32_e32 v16, 0xffff0000, v19
	ds_read_b32 v17, v52 offset:28
	v_and_b32_e32 v11, 0xffff0000, v11
	v_cndmask_b32_e64 v16, 0, v16, s[8:9]
	v_and_b32_e32 v15, 0xffff0000, v15
	v_cndmask_b32_e64 v15, 0, v15, s[10:11]
.Lfp3_join:
	v_sub_f32_e32 v16, v16, v11
	v_sub_f32_e32 v15, v15, v11
	v_fmac_f32_e32 v11, v16, v3
	v_exp_f32_e32 v16, v59
	s_waitcnt lgkmcnt(1)
	v_mul_f32_e32 v19, 0xbfb8aa3b, v60
	v_exp_f32_e32 v19, v19
	v_fmac_f32_e32 v11, v15, v7
	s_waitcnt lgkmcnt(0)
	v_add_f32_e32 v7, -1.0, v17
	v_mul_f32_e32 v15, 0x3fb8aa3b, v60
	v_mul_f32_e32 v3, v64, v24
	v_fma_f32 v7, v35, v7, 1.0
	v_exp_f32_e32 v15, v15
	v_mul_f32_e32 v7, v138, v7
	v_mul_f32_e64 v16, v16, -v3
	v_mul_f32_e32 v3, v3, v17
	v_mul_f32_e32 v17, v19, v3
	v_mul_f32_e32 v3, v11, v7
	v_fmac_f32_e32 v36, v31, v3
	v_cvt_pk_bf16_f32 v3, v25, v16
	v_mul_lo_u32 v16, v48, s39
	v_mul_f32_e32 v19, v19, v7
	v_mul_f32_e32 v15, v11, v15
	v_add3_u32 v16, v111, v16, v104
	v_cvt_pk_bf16_f32 v4, v21, v28
	v_cvt_pk_bf16_f32 v12, v20, v23
	v_cvt_pk_bf16_f32 v20, v98, v95
	v_cvt_pk_bf16_f32 v21, v100, v99
	v_cvt_pk_bf16_f32 v22, v102, v101
	v_cvt_pk_bf16_f32 v23, v110, v61
	v_cvt_pk_bf16_f32 v7, v26, v17
	v_cvt_pk_bf16_f32 v11, v18, v19
	v_cvt_pk_bf16_f32 v15, v27, v15
	ds_write_b128 v16, v[0:3]
	ds_write_b128 v16, v[4:7] offset:18432
	ds_write_b128 v16, v[8:11] offset:36864
	ds_write_b128 v16, v[12:15] offset:55296
	ds_write_b128 v16, v[20:23] offset:64512
	v_add_f32_dpp v0, v36, v36 quad_perm:[1,0,3,2] row_mask:0xf bank_mask:0xf bound_ctrl:1
	v_cmp_eq_u32_e32 vcc, 0, v137
	s_nop 0
	v_add_f32_dpp v0, v0, v0 quad_perm:[2,3,0,1] row_mask:0xf bank_mask:0xf bound_ctrl:1
	s_nop 1
	v_mov_b32_dpp v1, v0 row_half_mirror row_mask:0xf bank_mask:0xf bound_ctrl:1
	s_and_saveexec_b64 s[0:1], vcc
	s_cbranch_execz .LBB0_426
	s_mul_i32 s28, s26, 0x2200
	v_lshl_add_u64 v[2:3], v[96:97], 0, s[28:29]
	v_readlane_b32 s8, v255, 10
	v_lshlrev_b64 v[2:3], 6, v[2:3]
	v_readlane_b32 s9, v255, 11
	v_add_f32_e32 v4, v0, v1
	s_lshl_b32 s28, s40, 2
	v_lshl_add_u64 v[0:1], s[8:9], 0, v[2:3]
	v_lshl_add_u64 v[0:1], v[0:1], 0, s[28:29]
	global_store_dword v[0:1], v4, off

.Lfp1:
	s_waitcnt vmcnt(13)
	v_and_b32_e32 v97, 0xffff0000, v152
	v_lshlrev_b32_e32 v29, 16, v152
	v_sub_f32_e32 v30, v30, v145
	v_lshlrev_b32_e32 v104, 16, v149
	v_sub_f32_e32 v28, v28, v146
	v_sub_f32_e32 v97, v97, v145
	v_lshlrev_b32_e32 v147, 16, v153
	v_and_b32_e32 v148, 0xffff0000, v149
	s_waitcnt vmcnt(8)
	v_lshlrev_b32_e32 v170, 16, v64
	v_and_b32_e32 v64, 0xffff0000, v64
	v_sub_f32_e32 v172, v64, v95
	v_lshlrev_b32_e32 v64, 16, v65
	v_sub_f32_e32 v174, v64, v100
	v_and_b32_e32 v64, 0xffff0000, v65
	s_waitcnt vmcnt(6)
	v_and_b32_e32 v65, 0xffff0000, v69
	v_sub_f32_e32 v177, v65, v99
	v_lshlrev_b32_e32 v65, 16, v70
	v_sub_f32_e32 v179, v65, v102
	v_and_b32_e32 v65, 0xffff0000, v70
	v_sub_f32_e32 v181, v65, v101
	v_lshlrev_b32_e32 v65, 16, v71
	s_waitcnt lgkmcnt(7)
	v_fmac_f32_e32 v145, v30, v81
	v_lshlrev_b32_e32 v110, 16, v31
	v_sub_f32_e32 v29, v29, v146
	v_sub_f32_e32 v104, v104, v144
	v_and_b32_e32 v149, 0xffff0000, v153
	v_lshlrev_b32_e32 v152, 16, v150
	v_lshlrev_b32_e32 v171, 16, v68
	v_and_b32_e32 v68, 0xffff0000, v68
	v_sub_f32_e32 v176, v64, v99
	v_lshlrev_b32_e32 v64, 16, v66
	v_fmac_f32_e32 v146, v28, v80
	s_waitcnt lgkmcnt(5)
	v_fmac_f32_e32 v145, v97, v85
	v_sub_f32_e32 v147, v147, v144
	v_sub_f32_e32 v148, v148, v143
	v_lshlrev_b32_e32 v153, 16, v154
	v_and_b32_e32 v150, 0xffff0000, v150
	v_sub_f32_e32 v189, v65, v110
	v_fmac_f32_e32 v146, v29, v84
	v_fmac_f32_e32 v144, v104, v82
	s_waitcnt vmcnt(4)
	v_mul_f32_e32 v65, v161, v145
	v_sub_f32_e32 v149, v149, v143
	v_sub_f32_e32 v152, v152, v141
	v_and_b32_e32 v154, 0xffff0000, v154
	v_lshlrev_b32_e32 v168, 16, v151
	v_sub_f32_e32 v173, v68, v95
	v_lshlrev_b32_e32 v68, 16, v69
	v_sub_f32_e32 v178, v64, v102
	v_and_b32_e32 v64, 0xffff0000, v66
	v_fmac_f32_e32 v144, v147, v86
	v_fmac_f32_e32 v143, v148, v83
	v_mul_f32_e32 v66, v160, v146
	v_mul_f32_e32 v28, v65, v65
	v_sub_f32_e32 v153, v153, v141
	v_sub_f32_e32 v150, v150, v140
	v_lshlrev_b32_e32 v169, 16, v155
	v_and_b32_e32 v151, 0xffff0000, v151
	v_fmac_f32_e32 v143, v149, v87
	v_fmac_f32_e32 v141, v152, v72
	v_fmac_f32_e32 v28, v66, v66
	v_mul_f32_e32 v69, v162, v144
	v_sub_f32_e32 v154, v154, v140
	v_sub_f32_e32 v168, v168, v139
	v_and_b32_e32 v155, 0xffff0000, v155
	v_sub_f32_e32 v175, v68, v100
	s_waitcnt lgkmcnt(4)
	v_fmac_f32_e32 v141, v153, v76
	v_fmac_f32_e32 v140, v150, v73
	v_fmac_f32_e32 v28, v69, v69
	v_mul_f32_e32 v68, v163, v143
	v_sub_f32_e32 v169, v169, v139
	v_sub_f32_e32 v151, v151, v138
	v_fmac_f32_e32 v140, v154, v77
	v_fmac_f32_e32 v139, v168, v74
	v_fmac_f32_e32 v28, v68, v68
	v_mul_f32_e32 v72, v156, v141
	v_sub_f32_e32 v155, v155, v138
	v_sub_f32_e32 v180, v64, v101
	v_lshlrev_b32_e32 v64, 16, v67
	v_fmac_f32_e32 v139, v169, v78
	v_fmac_f32_e32 v138, v151, v75
	v_fmac_f32_e32 v28, v72, v72
	v_mul_f32_e32 v70, v157, v140
	v_fmac_f32_e32 v138, v155, v79
	v_fmac_f32_e32 v28, v70, v70
	v_mul_f32_e32 v73, v158, v139
	v_sub_f32_e32 v188, v64, v110
	v_fmac_f32_e32 v28, v73, v73
	v_mul_f32_e32 v64, v159, v138
	v_fmac_f32_e32 v28, v64, v64
	s_nop 0
	v_sub_f32_e32 v170, v170, v98
	v_add_f32_dpp v28, v28, v28 quad_perm:[1,0,3,2] row_mask:0xf bank_mask:0xf bound_ctrl:1
	v_sub_f32_e32 v171, v171, v98
	s_waitcnt lgkmcnt(3)
	v_fmac_f32_e32 v98, v170, v60
	v_fmac_f32_e32 v95, v172, v61
	v_fmac_f32_e32 v100, v174, v62
	v_fmac_f32_e32 v99, v176, v63
	s_waitcnt lgkmcnt(2)
	v_fmac_f32_e32 v102, v178, v32
	v_fmac_f32_e32 v101, v180, v33
	v_fmac_f32_e32 v110, v188, v34
	v_add_f32_dpp v62, v28, v28 quad_perm:[2,3,0,1] row_mask:0xf bank_mask:0xf bound_ctrl:1
	s_waitcnt lgkmcnt(1)
	v_fmac_f32_e32 v98, v171, v164
	v_fmac_f32_e32 v95, v173, v165
	v_mov_b32_dpp v63, v62 row_half_mirror row_mask:0xf bank_mask:0xf bound_ctrl:1
	v_fmac_f32_e32 v100, v175, v166
	v_fmac_f32_e32 v99, v177, v167
	s_waitcnt lgkmcnt(0)
	v_fmac_f32_e32 v102, v179, v88
	v_fmac_f32_e32 v101, v181, v89
	v_fmac_f32_e32 v110, v189, v90
	s_cbranch_vccnz .Lfp1_393
	s_mov_b64 s[0:1], 0
.Lfp1_393:
	v_and_b32_e32 v28, 0xffff0000, v67
	v_and_b32_e32 v61, 0xffff0000, v31
	v_and_b32_e32 v29, 0xffff0000, v71
	v_sub_f32_e32 v28, v28, v61
	v_lshlrev_b32_e32 v74, 3, v137
	v_sub_f32_e32 v29, v29, v61
	v_fmac_f32_e32 v61, v28, v35
	v_ashrrev_i32_e32 v97, 31, v96
	s_lshl_b32 s41, s40, 6
	v_fmac_f32_e32 v61, v29, v91
	s_andn2_b64 vcc, exec, s[0:1]
	v_lshlrev_b32_e32 v104, 1, v74
	s_cbranch_vccnz .Lfp1_395
	v_readlane_b32 s0, v255, 8
	v_lshlrev_b64 v[32:33], 11, v[96:97]
	v_readlane_b32 s1, v255, 9
	s_lshl_b32 s28, s41, 1
	v_cvt_pk_bf16_f32 v28, v98, v95
	v_lshl_add_u64 v[32:33], s[0:1], 0, v[32:33]
	v_lshl_add_u64 v[32:33], v[32:33], 0, s[28:29]
	v_cvt_pk_bf16_f32 v29, v100, v99
	v_cvt_pk_bf16_f32 v30, v102, v101
	v_cvt_pk_bf16_f32 v31, v110, v61
	v_lshl_add_u64 v[32:33], v[32:33], 0, v[104:105]
	global_store_dwordx4 v[32:33], v[28:31], off
.Lfp1_395:
	s_waitcnt vmcnt(2)
	v_lshlrev_b32_e32 v34, 16, v38
	v_and_b32_e32 v32, 0xffff0000, v38
	v_lshlrev_b32_e32 v30, 16, v39
	v_and_b32_e32 v28, 0xffff0000, v39
	v_and_b32_e32 v39, 0xffff0000, v59
	v_and_b32_e32 v38, 0xffff0000, v55
	v_lshlrev_b32_e32 v149, 16, v56
	v_lshlrev_b32_e32 v148, 16, v52
	v_and_b32_e32 v151, 0xffff0000, v56
	v_and_b32_e32 v150, 0xffff0000, v52
	v_lshlrev_b32_e32 v153, 16, v57
	v_lshlrev_b32_e32 v152, 16, v53
	v_and_b32_e32 v52, 0xffff0000, v53
	v_and_b32_e32 v53, 0xffff0000, v57
	v_lshlrev_b32_e32 v57, 16, v58
	v_lshlrev_b32_e32 v56, 16, v54
	v_and_b32_e32 v155, 0xffff0000, v58
	v_and_b32_e32 v154, 0xffff0000, v54
	v_lshlrev_b32_e32 v54, 16, v55
	v_lshlrev_b32_e32 v55, 16, v59
	s_waitcnt vmcnt(1)
	s_waitcnt vmcnt(0)
	v_lshlrev_b32_e32 v59, 16, v48
	v_lshlrev_b32_e32 v58, 16, v44
	v_and_b32_e32 v157, 0xffff0000, v48
	v_and_b32_e32 v156, 0xffff0000, v44
	v_lshlrev_b32_e32 v159, 16, v49
	v_lshlrev_b32_e32 v158, 16, v45
	v_and_b32_e32 v44, 0xffff0000, v45
	v_and_b32_e32 v45, 0xffff0000, v49
	v_lshlrev_b32_e32 v49, 16, v50
	v_lshlrev_b32_e32 v48, 16, v46
	v_and_b32_e32 v161, 0xffff0000, v50
	v_and_b32_e32 v160, 0xffff0000, v46
	v_lshlrev_b32_e32 v67, 2, v74
	v_lshlrev_b32_e32 v163, 16, v51
	v_lshlrev_b32_e32 v162, 16, v47
	v_and_b32_e32 v33, 0xffff0000, v51
	v_and_b32_e32 v35, 0xffff0000, v47
	v_add_u32_e32 v29, v117, v67
	v_lshlrev_b32_e32 v84, 16, v42
	v_and_b32_e32 v86, 0xffff0000, v42
	v_lshlrev_b32_e32 v60, 16, v36
	v_and_b32_e32 v42, 0xffff0000, v36
	v_and_b32_e32 v36, 0xffff0000, v37
	v_cndmask_b32_e64 v47, 0, v33, s[10:11]
	v_cndmask_b32_e64 v46, 0, v35, s[8:9]
	s_branch .Lfp1_join
.Lfp3:
	v_lshlrev_b32_e32 v89, 16, v12
	v_sub_f32_e32 v88, v88, v87
	v_and_b32_e32 v16, 0xffff0000, v16
	v_sub_f32_e32 v89, v89, v87
	v_fmac_f32_e32 v87, v88, v20
	v_add_f32_e32 v20, v62, v63
	v_and_b32_e32 v8, 0xffff0000, v8
	v_and_b32_e32 v12, 0xffff0000, v12
	v_max_f32_e32 v20, 0x179abe15, v20
	v_sub_f32_e32 v16, v16, v8
	v_fmac_f32_e32 v87, v89, v24
	v_rsq_f32_e32 v24, v20
	s_waitcnt lgkmcnt(13)
	v_add_f32_e32 v20, -1.0, v57
	v_sub_f32_e32 v12, v12, v8
	v_fmac_f32_e32 v8, v16, v21
	v_fma_f32 v20, v40, v20, 1.0
	v_fmac_f32_e32 v8, v12, v25
	s_waitcnt lgkmcnt(11)
	v_add_f32_e32 v12, -1.0, v58
	v_mul_f32_e32 v20, v146, v20
	v_fma_f32 v12, v41, v12, 1.0
	v_mul_f32_e32 v40, v87, v20
	v_mul_f32_e32 v12, v145, v12
	v_fma_f32 v36, v36, v40, 0
	v_mul_f32_e32 v16, v8, v12
	v_lshlrev_b32_e32 v21, 16, v17
	v_and_b32_e32 v17, 0xffff0000, v17
	v_fmac_f32_e32 v36, v37, v16
	v_lshlrev_b32_e32 v16, 16, v9
	v_lshlrev_b32_e32 v25, 16, v13
	v_and_b32_e32 v9, 0xffff0000, v9
	v_and_b32_e32 v13, 0xffff0000, v13
	v_sub_f32_e32 v21, v21, v16
	v_sub_f32_e32 v17, v17, v9
	v_sub_f32_e32 v25, v25, v16
	v_fmac_f32_e32 v16, v21, v22
	s_waitcnt lgkmcnt(9)
	v_add_f32_e32 v21, -1.0, v76
	v_sub_f32_e32 v13, v13, v9
	v_fmac_f32_e32 v9, v17, v23
	v_fma_f32 v21, v42, v21, 1.0
	v_fmac_f32_e32 v9, v13, v27
	s_waitcnt lgkmcnt(7)
	v_add_f32_e32 v13, -1.0, v77
	v_fmac_f32_e32 v16, v25, v26
	v_mul_f32_e32 v21, v144, v21
	v_fma_f32 v13, v43, v13, 1.0
	v_mul_f32_e32 v22, v16, v21
	v_mul_f32_e32 v13, v143, v13
	v_fmac_f32_e32 v36, v38, v22
	v_mul_f32_e32 v17, v9, v13
	v_lshlrev_b32_e32 v22, 16, v18
	v_fmac_f32_e32 v36, v39, v17
	v_lshlrev_b32_e32 v17, 16, v10
	v_lshlrev_b32_e32 v23, 16, v14
	v_sub_f32_e32 v22, v22, v17
	v_sub_f32_e32 v23, v23, v17
	v_fmac_f32_e32 v17, v22, v0
	s_waitcnt lgkmcnt(5)
	v_add_f32_e32 v0, -1.0, v82
	v_fma_f32 v0, v32, v0, 1.0
	v_fmac_f32_e32 v17, v23, v4
	v_mul_f32_e32 v0, v141, v0
	v_mul_f32_e32 v4, v17, v0
	v_fmac_f32_e32 v36, v28, v4
	v_and_b32_e32 v4, 0xffff0000, v10
	v_and_b32_e32 v10, 0xffff0000, v18
	v_and_b32_e32 v14, 0xffff0000, v14
	v_sub_f32_e32 v10, v10, v4
	v_sub_f32_e32 v14, v14, v4
	v_fmac_f32_e32 v4, v10, v1
	s_waitcnt lgkmcnt(3)
	v_add_f32_e32 v1, -1.0, v83
	v_fma_f32 v1, v33, v1, 1.0
	v_fmac_f32_e32 v4, v14, v5
	v_mul_f32_e32 v1, v140, v1
	v_mul_f32_e32 v5, v4, v1
	v_lshlrev_b32_e32 v10, 16, v19
	v_fmac_f32_e32 v36, v29, v5
	v_lshlrev_b32_e32 v5, 16, v11
	v_lshlrev_b32_e32 v14, 16, v15
	v_sub_f32_e32 v10, v10, v5
	v_sub_f32_e32 v14, v14, v5
	v_fmac_f32_e32 v5, v10, v2
	v_fmac_f32_e32 v5, v14, v6
	s_waitcnt lgkmcnt(2)
	v_mul_f32_e32 v10, 0x3fb8aa3b, v84
	v_exp_f32_e32 v14, v85
	v_mul_f32_e32 v18, 0xbfb8aa3b, v84
	v_exp_f32_e32 v18, v18
	v_exp_f32_e32 v10, v10
	s_waitcnt lgkmcnt(1)
	v_add_f32_e32 v6, -1.0, v86
	v_mul_f32_e32 v2, v73, v24
	v_fma_f32 v6, v34, v6, 1.0
	v_mul_f32_e32 v6, v139, v6
	v_mul_f32_e64 v25, v14, -v2
	v_mul_f32_e32 v2, v2, v86
	v_mul_f32_e32 v26, v18, v2
	v_mul_f32_e32 v18, v18, v6
	v_mul_f32_e32 v27, v5, v10
	v_mul_f32_e32 v2, v5, v6
	v_mul_f32_e32 v5, 0x3fb8aa3b, v79
	v_exp_f32_e32 v6, v81
	v_mul_f32_e32 v10, 0xbfb8aa3b, v79
	v_exp_f32_e32 v10, v10
	v_exp_f32_e32 v5, v5
	v_fmac_f32_e32 v36, v30, v2
	v_mul_f32_e32 v2, v72, v24
	v_mul_f32_e64 v6, v6, -v2
	v_mul_f32_e32 v2, v2, v82
	v_mul_f32_e32 v14, v10, v2
	v_mul_f32_e32 v0, v10, v0
	v_mul_f32_e32 v5, v17, v5
	v_mul_f32_e32 v10, 0x3fb8aa3b, v80
	v_exp_f32_e32 v17, v78
	v_mul_f32_e32 v22, 0xbfb8aa3b, v80
	v_exp_f32_e32 v22, v22
	v_exp_f32_e32 v10, v10
	v_mul_f32_e32 v2, v70, v24
	v_mul_f32_e64 v17, v17, -v2
	v_mul_f32_e32 v2, v2, v83
	v_mul_f32_e32 v23, v22, v2
	v_mul_f32_e32 v4, v4, v10
	v_cvt_pk_bf16_f32 v2, v6, v17
	v_cvt_pk_bf16_f32 v6, v14, v23
	v_cvt_pk_bf16_f32 v14, v5, v4
	v_exp_f32_e32 v4, v75
	v_mul_f32_e32 v5, 0xbfb8aa3b, v71
	v_exp_f32_e32 v5, v5
	v_mul_f32_e32 v1, v22, v1
	v_cvt_pk_bf16_f32 v10, v0, v1
	v_mul_f32_e32 v0, v69, v24
	v_mul_f32_e32 v1, 0x3fb8aa3b, v71
	v_exp_f32_e32 v1, v1
	v_mul_f32_e64 v4, v4, -v0
	v_mul_f32_e32 v0, v0, v76
	v_mul_f32_e32 v0, v5, v0
	v_mul_f32_e32 v17, v5, v21
	v_mul_f32_e32 v5, 0x3fb8aa3b, v74
	v_exp_f32_e32 v21, v67
	v_mul_f32_e32 v22, 0xbfb8aa3b, v74
	v_exp_f32_e32 v22, v22
	v_exp_f32_e32 v5, v5
	v_mul_f32_e32 v16, v16, v1
	v_mul_f32_e32 v1, v68, v24
	v_mul_f32_e64 v21, v21, -v1
	v_mul_f32_e32 v1, v1, v77
	v_mul_f32_e32 v23, v22, v1
	v_mul_f32_e32 v13, v22, v13
	v_mul_f32_e32 v22, v9, v5
	v_cvt_pk_bf16_f32 v1, v4, v21
	v_cvt_pk_bf16_f32 v9, v17, v13
	v_cvt_pk_bf16_f32 v13, v16, v22
	v_mul_f32_e32 v4, 0x3fb8aa3b, v54
	v_exp_f32_e32 v16, v56
	v_mul_f32_e32 v17, 0xbfb8aa3b, v54
	v_exp_f32_e32 v17, v17
	v_exp_f32_e32 v4, v4
	v_cvt_pk_bf16_f32 v5, v0, v23
	v_mul_f32_e32 v0, v66, v24
	v_mul_f32_e64 v16, v16, -v0
	v_mul_f32_e32 v0, v0, v57
	v_mul_f32_e32 v23, 0xbfb8aa3b, v55
	v_mul_f32_e32 v21, v17, v0
	v_mul_f32_e32 v17, v17, v20
	v_mul_f32_e32 v20, v87, v4
	v_mul_f32_e32 v4, 0x3fb8aa3b, v55
	v_exp_f32_e32 v22, v53
	v_exp_f32_e32 v23, v23
	v_exp_f32_e32 v4, v4
	v_mul_f32_e32 v0, v65, v24
	v_mul_f32_e64 v22, v22, -v0
	v_mul_f32_e32 v0, v0, v58
	v_mul_f32_e32 v12, v23, v12
	v_mul_f32_e32 v28, v23, v0
	v_mul_f32_e32 v23, v8, v4
	v_cvt_pk_bf16_f32 v0, v16, v22
	v_cvt_pk_bf16_f32 v8, v17, v12
	v_and_b32_e32 v16, 0xffff0000, v19
	ds_read_b32 v17, v52 offset:28
	v_and_b32_e32 v11, 0xffff0000, v11
	v_and_b32_e32 v15, 0xffff0000, v15
	s_branch .Lfp3_join
